# one static priority raise for waves 4-7 across the indexer + masked attention and the stick-breaking attention phases
# baseline (speedup 1.0000x reference)
; __device__ __forceinline__ int lane_id() { int l; asm volatile("v_mbcnt_lo_u32_b32 %0, -1, 0\n\tv_mbcnt_hi_u32_b32 %0, -1, %0" : "=v"(l)); return l; }
; __device__ __forceinline__ Frame make_frame(int wave_s) {
;     Frame F; F.lds = LDS0; { int t_ = wave_s * 64 + lane_id(); asm volatile("" : "+v"(t_)); F.tid = t_; } F.lane = F.tid & 63; F.wave = wave_s;
;     F.G = gridDim.x; { const int bx = blockIdx.x; F.vcu = (F.G % 8 == 0) ? (bx % 8) * (F.G / 8) + bx / 8 : bx; }
;     return F;
.LBB0_346:
	s_or_b64 exec, exec, s[4:5]
	s_waitcnt lgkmcnt(0)
	s_barrier
	s_cmp_lt_u32 s78, 4
	s_cbranch_scc1 .Lhp_o_skip
	s_setprio 1
.Lhp_o_skip:
	v_mbcnt_lo_u32_b32 v0, -1, 0
	v_mbcnt_hi_u32_b32 v0, -1, v0
	s_andn2_b64 vcc, exec, s[42:43]
	v_add_u32_e32 v3, s79, v0
	s_mov_b32 s82, s74
	s_cbranch_vccnz .LBB0_348
	v_readlane_b32 s0, v255, 6
	s_ashr_i32 s0, s0, 3
	v_readlane_b32 s1, v254, 22
	s_mul_i32 s0, s0, s1
	v_readlane_b32 s1, v254, 19
	s_add_i32 s82, s0, s1

; #define LAS __attribute__((address_space(3)))
; __device__ __forceinline__ int lane_id() { int l; asm volatile("v_mbcnt_lo_u32_b32 %0, -1, 0\n\tv_mbcnt_hi_u32_b32 %0, -1, %0" : "=v"(l)); return l; }
; __device__ __forceinline__ unsigned xb_xcc_id() { return (unsigned)__builtin_amdgcn_s_getreg((3 << 11) | 20) & 0xFu; }
; __device__ __forceinline__ unsigned char* karg_ws() { return (unsigned char*)(GAS unsigned char*)karg_u64<15>(); }
; __device__ __forceinline__ void grid_barrier(int wave_s) {
;     XcdBarrier b; b.bar = (unsigned*)(karg_ws() + WS_CTL) + 4096; b.x = xb_xcc_id(); b.st = (volatile LAS unsigned*)(LDS0 + MISC_OFF) + 8;
;     xcd_barrier_impl(b, wave_s == 0 && lane_id() == 0);
.LBB0_373:
	v_readlane_b32 s76, v254, 59
	v_readlane_b32 s77, v254, 60
	s_load_dwordx2 s[6:7], s[76:77], 0x78
	s_waitcnt lgkmcnt(0)
	v_readlane_b32 s0, v255, 7
	v_readlane_b32 s1, v255, 8
	s_mov_b64 s[8:9], 0
	s_and_b64 vcc, exec, s[0:1]
	s_setprio 0
	s_getreg_b32 s0, hwreg(HW_REG_XCC_ID, 0, 4)
	s_cbranch_vccnz .LBB0_375
	v_mbcnt_lo_u32_b32 v0, -1, 0
	v_mbcnt_hi_u32_b32 v0, -1, v0
	s_nop 0
	v_cmp_eq_u32_e32 vcc, 0, v0
	s_and_b64 s[8:9], vcc, exec

; __device__ __forceinline__ int lane_id() { int l; asm volatile("v_mbcnt_lo_u32_b32 %0, -1, 0\n\tv_mbcnt_hi_u32_b32 %0, -1, %0" : "=v"(l)); return l; }
; __device__ __forceinline__ Frame make_frame(int wave_s) {
;     Frame F; F.lds = LDS0; { int t_ = wave_s * 64 + lane_id(); asm volatile("" : "+v"(t_)); F.tid = t_; } F.lane = F.tid & 63; F.wave = wave_s;
;     F.G = gridDim.x; { const int bx = blockIdx.x; F.vcu = (F.G % 8 == 0) ? (bx % 8) * (F.G / 8) + bx / 8 : bx; }
;     return F;
.Lhp_e_skip:
	v_mbcnt_lo_u32_b32 v0, -1, 0
	v_mbcnt_hi_u32_b32 v0, -1, v0
	s_mov_b32 s57, s74
	v_add_u32_e32 v212, s79, v0
	s_load_dword s56, s[82:83], 0x0
	s_waitcnt lgkmcnt(0)
	s_and_b32 s0, s56, 7
	s_cmp_eq_u32 s0, 0
	s_cselect_b64 s[24:25], -1, 0
	s_cmp_lg_u32 s0, 0
	s_cbranch_scc1 .LBB0_694
	s_ashr_i32 s0, s56, 3
	v_readlane_b32 s1, v254, 22
	s_mul_i32 s0, s0, s1
	v_readlane_b32 s1, v254, 19
	s_add_i32 s57, s0, s1

; #define LAS __attribute__((address_space(3)))
; __device__ __forceinline__ int lane_id() { int l; asm volatile("v_mbcnt_lo_u32_b32 %0, -1, 0\n\tv_mbcnt_hi_u32_b32 %0, -1, %0" : "=v"(l)); return l; }
; __device__ __forceinline__ unsigned xb_xcc_id() { return (unsigned)__builtin_amdgcn_s_getreg((3 << 11) | 20) & 0xFu; }
; __device__ __forceinline__ unsigned char* karg_ws() { return (unsigned char*)(GAS unsigned char*)karg_u64<15>(); }
; __device__ __forceinline__ void grid_barrier(int wave_s) {
;     XcdBarrier b; b.bar = (unsigned*)(karg_ws() + WS_CTL) + 4096; b.x = xb_xcc_id(); b.st = (volatile LAS unsigned*)(LDS0 + MISC_OFF) + 8;
;     xcd_barrier_impl(b, wave_s == 0 && lane_id() == 0);
.LBB0_1795:
	s_setprio 0
	s_load_dwordx2 s[6:7], s[76:77], 0x78
	s_waitcnt lgkmcnt(0)
	s_mov_b64 s[8:9], 0
	s_andn2_b64 vcc, exec, s[80:81]
	s_getreg_b32 s0, hwreg(HW_REG_XCC_ID, 0, 4)
	s_cbranch_vccnz .LBB0_1797
	v_mbcnt_lo_u32_b32 v0, -1, 0
	v_mbcnt_hi_u32_b32 v0, -1, v0
	s_nop 0
	v_cmp_eq_u32_e32 vcc, 0, v0
	s_and_b64 s[8:9], vcc, exec
